# attention: dropped hipcc's mid-chunk vmcnt(0) drains in front of the V LDS reads (next chunk's K/V loads stay in flight); on top of v24
# baseline (speedup 1.0000x reference)
.LBB0_623:
	v_sub_f32_e32 v74, v205, v188
	v_exp_f32_e32 v80, v74
	v_sub_f32_e32 v74, v204, v188
	v_exp_f32_e32 v81, v74
	v_sub_f32_e32 v74, v203, v188
	v_exp_f32_e32 v218, v74
	v_sub_f32_e32 v74, v202, v188
	v_exp_f32_e32 v219, v74
	v_sub_f32_e32 v74, v201, v188
	v_exp_f32_e32 v201, v74
	v_sub_f32_e32 v74, v199, v188
	v_sub_f32_e32 v71, v71, v188
	v_exp_f32_e32 v199, v74
	v_sub_f32_e32 v74, v198, v188
	v_exp_f32_e32 v222, v71
	v_add3_u32 v71, s22, v159, v172
	v_exp_f32_e32 v198, v74
	v_sub_f32_e32 v74, v197, v188
	v_add_u32_e32 v206, v71, v171
	v_exp_f32_e32 v197, v74
	v_add_u32_e32 v207, v71, v173
	ds_read_b64_tr_b16 v[76:77], v206 offset:16384
	ds_read_b64_tr_b16 v[78:79], v207 offset:18432
	v_add_u32_e32 v210, v71, v174
	v_sub_f32_e32 v73, v73, v188
	v_sub_f32_e32 v72, v72, v188
	v_add_u32_e32 v211, v71, v175
	ds_read_b64_tr_b16 v[202:203], v210 offset:16384
	ds_read_b64_tr_b16 v[204:205], v211 offset:18432
	ds_read_b64_tr_b16 v[208:209], v207 offset:22528
	ds_read_b64_tr_b16 v[206:207], v206 offset:20480
	v_exp_f32_e32 v220, v73
	v_exp_f32_e32 v221, v72
	v_cvt_pk_bf16_f32 v72, v80, v81
	v_cvt_pk_bf16_f32 v73, v218, v219
	v_cvt_pk_bf16_f32 v74, v201, v199
	v_cvt_pk_bf16_f32 v75, v198, v197
	v_add_u32_e32 v214, v71, v176
	v_sub_f32_e32 v70, v70, v188
	s_waitcnt lgkmcnt(4)
	v_mfma_f32_32x32x16_bf16 v[50:65], v[76:79], v[72:75], v[50:65]
	v_add_u32_e32 v215, v71, v177
	ds_read_b64_tr_b16 v[76:77], v214 offset:16384
	ds_read_b64_tr_b16 v[78:79], v215 offset:18432
	ds_read_b64_tr_b16 v[212:213], v211 offset:22528
	ds_read_b64_tr_b16 v[210:211], v210 offset:20480
	v_add_u32_e32 v224, v71, v178
	v_exp_f32_e32 v223, v70
	v_add_u32_e32 v70, v71, v179
	v_sub_f32_e32 v69, v69, v188
	v_sub_f32_e32 v68, v68, v188
	s_waitcnt lgkmcnt(6)
	v_mfma_f32_32x32x16_bf16 v[34:49], v[202:205], v[72:75], v[34:49]
	ds_read_b64_tr_b16 v[202:203], v224 offset:16384
	ds_read_b64_tr_b16 v[204:205], v70 offset:18432
	ds_read_b64_tr_b16 v[216:217], v215 offset:22528
	ds_read_b64_tr_b16 v[214:215], v214 offset:20480
	v_sub_f32_e32 v67, v67, v188
	v_sub_f32_e32 v66, v66, v188
	v_exp_f32_e32 v67, v67
	v_exp_f32_e32 v66, v66
	s_waitcnt lgkmcnt(6)
	v_mfma_f32_32x32x16_bf16 v[18:33], v[76:79], v[72:75], v[18:33]
	v_add_f32_e32 v78, 0, v80
	v_add_f32_e32 v78, v78, v81
	v_add_f32_e32 v78, v78, v218
	v_add_f32_e32 v78, v78, v219
	v_exp_f32_e32 v76, v69
	v_exp_f32_e32 v77, v68
	ds_read_b64_tr_b16 v[70:71], v70 offset:22528
	ds_read_b64_tr_b16 v[68:69], v224 offset:20480
	s_waitcnt lgkmcnt(4)
	v_mfma_f32_32x32x16_bf16 v[2:17], v[202:205], v[72:75], v[2:17]
	v_add_f32_e32 v78, v78, v201
	v_add_f32_e32 v78, v78, v199
	v_add_f32_e32 v78, v78, v198
	v_add_f32_e32 v78, v78, v197
	v_cvt_pk_bf16_f32 v72, v220, v221
	v_cvt_pk_bf16_f32 v73, v222, v223
	v_cvt_pk_bf16_f32 v74, v76, v77
	v_cvt_pk_bf16_f32 v75, v67, v66
	v_add_f32_e32 v78, v78, v220
	v_add_f32_e32 v78, v78, v221
	v_mfma_f32_32x32x16_bf16 v[50:65], v[206:209], v[72:75], v[50:65]
	v_add_f32_e32 v78, v78, v222
	v_add_f32_e32 v78, v78, v223
	v_add_f32_e32 v76, v78, v76
	v_add_f32_e32 v76, v76, v77
	v_add_f32_e32 v67, v76, v67
	v_add_f32_e32 v66, v67, v66
	v_add_f32_e32 v143, v143, v66
	v_mfma_f32_32x32x16_bf16 v[34:49], v[210:213], v[72:75], v[34:49]
	s_waitcnt lgkmcnt(2)
	v_mfma_f32_32x32x16_bf16 v[18:33], v[214:217], v[72:75], v[18:33]
	s_waitcnt lgkmcnt(0)
	v_mfma_f32_32x32x16_bf16 v[2:17], v[68:71], v[72:75], v[2:17]

.LBB0_627:
	v_sub_f32_e32 v74, v196, v188
	v_exp_f32_e32 v80, v74
	v_sub_f32_e32 v74, v195, v188
	v_exp_f32_e32 v81, v74
	v_sub_f32_e32 v74, v194, v188
	v_exp_f32_e32 v198, v74
	v_sub_f32_e32 v74, v193, v188
	v_exp_f32_e32 v199, v74
	v_sub_f32_e32 v74, v192, v188
	v_exp_f32_e32 v201, v74
	v_sub_f32_e32 v74, v191, v188
	v_sub_f32_e32 v71, v71, v188
	v_exp_f32_e32 v210, v74
	v_sub_f32_e32 v74, v190, v188
	v_exp_f32_e32 v214, v71
	v_add3_u32 v71, s22, v159, v172
	v_exp_f32_e32 v211, v74
	v_sub_f32_e32 v74, v189, v188
	v_add_u32_e32 v194, v71, v171
	v_exp_f32_e32 v189, v74
	v_add_u32_e32 v195, v71, v173
	ds_read_b64_tr_b16 v[76:77], v194 offset:24576
	ds_read_b64_tr_b16 v[78:79], v195 offset:26624
	v_add_u32_e32 v202, v71, v174
	v_sub_f32_e32 v73, v73, v188
	v_sub_f32_e32 v72, v72, v188
	v_add_u32_e32 v203, v71, v175
	ds_read_b64_tr_b16 v[190:191], v202 offset:24576
	ds_read_b64_tr_b16 v[192:193], v203 offset:26624
	ds_read_b64_tr_b16 v[196:197], v195 offset:30720
	ds_read_b64_tr_b16 v[194:195], v194 offset:28672
	v_exp_f32_e32 v212, v73
	v_exp_f32_e32 v213, v72
	v_cvt_pk_bf16_f32 v72, v80, v81
	v_cvt_pk_bf16_f32 v73, v198, v199
	v_cvt_pk_bf16_f32 v74, v201, v210
	v_cvt_pk_bf16_f32 v75, v211, v189
	v_add_u32_e32 v206, v71, v176
	v_sub_f32_e32 v70, v70, v188
	s_waitcnt lgkmcnt(4)
	v_mfma_f32_32x32x16_bf16 v[50:65], v[76:79], v[72:75], v[50:65]
	v_add_u32_e32 v207, v71, v177
	ds_read_b64_tr_b16 v[76:77], v206 offset:24576
	ds_read_b64_tr_b16 v[78:79], v207 offset:26624
	ds_read_b64_tr_b16 v[204:205], v203 offset:30720
	ds_read_b64_tr_b16 v[202:203], v202 offset:28672
	v_add_u32_e32 v216, v71, v178
	v_exp_f32_e32 v215, v70
	v_add_u32_e32 v70, v71, v179
	v_sub_f32_e32 v69, v69, v188
	v_sub_f32_e32 v68, v68, v188
	s_waitcnt lgkmcnt(6)
	v_mfma_f32_32x32x16_bf16 v[34:49], v[190:193], v[72:75], v[34:49]
	ds_read_b64_tr_b16 v[190:191], v216 offset:24576
	ds_read_b64_tr_b16 v[192:193], v70 offset:26624
	ds_read_b64_tr_b16 v[208:209], v207 offset:30720
	ds_read_b64_tr_b16 v[206:207], v206 offset:28672
	v_sub_f32_e32 v67, v67, v188
	v_sub_f32_e32 v66, v66, v188
	v_exp_f32_e32 v67, v67
	v_exp_f32_e32 v66, v66
	s_waitcnt lgkmcnt(6)
	v_mfma_f32_32x32x16_bf16 v[18:33], v[76:79], v[72:75], v[18:33]
	v_add_f32_e32 v78, 0, v80
	v_add_f32_e32 v78, v78, v81
	v_add_f32_e32 v78, v78, v198
	v_add_f32_e32 v78, v78, v199
	v_exp_f32_e32 v76, v69
	v_exp_f32_e32 v77, v68
	ds_read_b64_tr_b16 v[70:71], v70 offset:30720
	ds_read_b64_tr_b16 v[68:69], v216 offset:28672
	s_waitcnt lgkmcnt(4)
	v_mfma_f32_32x32x16_bf16 v[2:17], v[190:193], v[72:75], v[2:17]
	v_add_f32_e32 v78, v78, v201
	v_add_f32_e32 v78, v78, v210
	v_add_f32_e32 v78, v78, v211
	v_add_f32_e32 v78, v78, v189
	v_cvt_pk_bf16_f32 v72, v212, v213
	v_cvt_pk_bf16_f32 v73, v214, v215
	v_cvt_pk_bf16_f32 v74, v76, v77
	v_cvt_pk_bf16_f32 v75, v67, v66
	v_add_f32_e32 v78, v78, v212
	v_add_f32_e32 v78, v78, v213
	v_mfma_f32_32x32x16_bf16 v[50:65], v[194:197], v[72:75], v[50:65]
	v_add_f32_e32 v78, v78, v214
	v_add_f32_e32 v78, v78, v215
	v_add_f32_e32 v76, v78, v76
	v_add_f32_e32 v76, v76, v77
	v_add_f32_e32 v67, v76, v67
	v_add_f32_e32 v66, v67, v66
	v_add_f32_e32 v143, v143, v66
	v_mfma_f32_32x32x16_bf16 v[34:49], v[202:205], v[72:75], v[34:49]
	s_waitcnt lgkmcnt(2)
	v_mfma_f32_32x32x16_bf16 v[18:33], v[206:209], v[72:75], v[18:33]
	s_waitcnt lgkmcnt(0)
	v_mfma_f32_32x32x16_bf16 v[2:17], v[68:71], v[72:75], v[2:17]
